# v117 plus: the XCC leader no longer waits for its cross-XCC generation add before releasing its own XCC's workgroups
# speedup vs baseline: 1.0104x; 1.0017x over previous
.LBB0_72:
	s_or_b64 exec, exec, s[8:9]
	s_mov_b64 s[8:9], exec
	v_mbcnt_lo_u32_b32 v1, s8, 0
	v_mbcnt_hi_u32_b32 v1, s9, v1
	v_cmp_eq_u32_e32 vcc, 0, v1
	s_and_saveexec_b64 s[12:13], vcc
	s_cbranch_execz .LBB0_74
	s_bcnt1_i32_b64 s0, s[8:9]
	v_mov_b32_e32 v1, 0x2000
	v_mov_b32_e32 v2, s0
	global_atomic_add v1, v2, s[10:11] offset:1024

.LBB0_1372:
	s_or_b64 exec, exec, s[10:11]
	s_mov_b64 s[10:11], exec
	v_mbcnt_lo_u32_b32 v1, s10, 0
	v_mbcnt_hi_u32_b32 v1, s11, v1
	v_cmp_eq_u32_e32 vcc, 0, v1
	s_and_saveexec_b64 s[14:15], vcc
	s_cbranch_execz .LBB0_1374
	s_bcnt1_i32_b64 s0, s[10:11]
	v_mov_b32_e32 v1, 0x2000
	v_mov_b32_e32 v2, s0
	global_atomic_add v1, v2, s[12:13] offset:1024

.LBB0_1607:
	s_or_b64 exec, exec, s[12:13]
	s_mov_b64 s[12:13], exec
	v_mbcnt_lo_u32_b32 v1, s12, 0
	v_mbcnt_hi_u32_b32 v1, s13, v1
	v_cmp_eq_u32_e32 vcc, 0, v1
	s_and_saveexec_b64 s[16:17], vcc
	s_cbranch_execz .LBB0_1609
	s_bcnt1_i32_b64 s12, s[12:13]
	v_mov_b32_e32 v1, 0x2000
	v_mov_b32_e32 v2, s12
	global_atomic_add v1, v2, s[14:15] offset:1024

.LBB0_1729:
	s_or_b64 exec, exec, s[4:5]
	s_mov_b64 s[4:5], exec
	v_mbcnt_lo_u32_b32 v1, s4, 0
	v_mbcnt_hi_u32_b32 v1, s5, v1
	v_cmp_eq_u32_e32 vcc, 0, v1
	s_and_saveexec_b64 s[10:11], vcc
	s_cbranch_execz .LBB0_1731
	s_bcnt1_i32_b64 s0, s[4:5]
	v_mov_b32_e32 v1, 0x2000
	v_mov_b32_e32 v2, s0
	global_atomic_add v1, v2, s[8:9] offset:1024
